# P0 w_in transpose: the 16 row loads of an item issued together with counted waits instead of one wait per load
# baseline (speedup 1.0000x reference)
; #define LAS __attribute__((address_space(3)))
; __device__ __forceinline__ void p0_tr_item(const float* W, int ldw, int k0, int n0, int nvalid, bf16* WT, int dst_row0, LAS float* scr, int lane) {
;     const int c4 = (lane & 15) * 4, kr = lane >> 4;
; #pragma unroll 4
;     for (int i = 0; i < 16; ++i) { const int kk = 4 * i + kr;
;         f32x4 v = (f32x4){0.f, 0.f, 0.f, 0.f};
;         if (c4 < nvalid) v = *(const f32x4*)(W + (size_t)(k0 + kk) * ldw + n0 + c4);
;         LAS float* d = scr + kk * 65 + c4; d[0] = v[0]; d[1] = v[1]; d[2] = v[2]; d[3] = v[3]; }
.LBB0_16:
	s_ashr_i32 s10, s16, 31
	s_lshr_b32 s10, s10, 26
	s_add_i32 s10, s16, s10
	s_and_b32 s12, s10, 0xffffffc0
	s_sub_i32 s10, s16, s12
	s_lshl_b32 s10, s10, 6
	s_ashr_i32 s11, s10, 31
	v_cmp_lt_i32_e32 vcc, s10, v14
	v_lshl_add_u64 v[12:13], s[10:11], 2, v[10:11]
	v_or_b32_e32 v28, s12, v1
	v_mov_b32_e32 v29, v25
	s_mov_b32 s11, 0
	v_mov_b64_e32 v[116:117], 0
	v_mov_b64_e32 v[118:119], 0
	v_mov_b64_e32 v[120:121], 0
	v_mov_b64_e32 v[122:123], 0
	v_mov_b64_e32 v[124:125], 0
	v_mov_b64_e32 v[126:127], 0
	v_mov_b64_e32 v[128:129], 0
	v_mov_b64_e32 v[130:131], 0
	v_mov_b64_e32 v[132:133], 0
	v_mov_b64_e32 v[134:135], 0
	v_mov_b64_e32 v[136:137], 0
	v_mov_b64_e32 v[138:139], 0
	v_mov_b64_e32 v[140:141], 0
	v_mov_b64_e32 v[142:143], 0
	v_mov_b64_e32 v[144:145], 0
	v_mov_b64_e32 v[146:147], 0
	v_mov_b64_e32 v[148:149], 0
	v_mov_b64_e32 v[150:151], 0
	v_mov_b64_e32 v[152:153], 0
	v_mov_b64_e32 v[154:155], 0
	v_mov_b64_e32 v[156:157], 0
	v_mov_b64_e32 v[158:159], 0
	v_mov_b64_e32 v[160:161], 0
	v_mov_b64_e32 v[162:163], 0
	v_mov_b64_e32 v[164:165], 0
	v_mov_b64_e32 v[166:167], 0
	v_mov_b64_e32 v[168:169], 0
	v_mov_b64_e32 v[170:171], 0
	v_mov_b64_e32 v[172:173], 0
	v_mov_b64_e32 v[174:175], 0
	v_mov_b64_e32 v[176:177], 0
	v_mov_b64_e32 v[178:179], 0
	s_and_saveexec_b64 s[14:15], vcc
	s_cbranch_execz .Ltr_ld_done
	v_mov_b32_e32 v3, v28
	v_mad_i64_i32 v[4:5], s[18:19], v3, s2, v[12:13]
	global_load_dwordx4 v[116:119], v[4:5], off
	v_add_u32_e32 v3, 4, v28
	v_mad_i64_i32 v[4:5], s[18:19], v3, s2, v[12:13]
	global_load_dwordx4 v[120:123], v[4:5], off
	v_add_u32_e32 v3, 8, v28
	v_mad_i64_i32 v[4:5], s[18:19], v3, s2, v[12:13]
	global_load_dwordx4 v[124:127], v[4:5], off
	v_add_u32_e32 v3, 12, v28
	v_mad_i64_i32 v[4:5], s[18:19], v3, s2, v[12:13]
	global_load_dwordx4 v[128:131], v[4:5], off
	v_add_u32_e32 v3, 16, v28
	v_mad_i64_i32 v[4:5], s[18:19], v3, s2, v[12:13]
	global_load_dwordx4 v[132:135], v[4:5], off
	v_add_u32_e32 v3, 20, v28
	v_mad_i64_i32 v[4:5], s[18:19], v3, s2, v[12:13]
	global_load_dwordx4 v[136:139], v[4:5], off
	v_add_u32_e32 v3, 24, v28
	v_mad_i64_i32 v[4:5], s[18:19], v3, s2, v[12:13]
	global_load_dwordx4 v[140:143], v[4:5], off
	v_add_u32_e32 v3, 28, v28
	v_mad_i64_i32 v[4:5], s[18:19], v3, s2, v[12:13]
	global_load_dwordx4 v[144:147], v[4:5], off
	v_add_u32_e32 v3, 32, v28
	v_mad_i64_i32 v[4:5], s[18:19], v3, s2, v[12:13]
	global_load_dwordx4 v[148:151], v[4:5], off
	v_add_u32_e32 v3, 36, v28
	v_mad_i64_i32 v[4:5], s[18:19], v3, s2, v[12:13]
	global_load_dwordx4 v[152:155], v[4:5], off
	v_add_u32_e32 v3, 40, v28
	v_mad_i64_i32 v[4:5], s[18:19], v3, s2, v[12:13]
	global_load_dwordx4 v[156:159], v[4:5], off
	v_add_u32_e32 v3, 44, v28
	v_mad_i64_i32 v[4:5], s[18:19], v3, s2, v[12:13]
	global_load_dwordx4 v[160:163], v[4:5], off
	v_add_u32_e32 v3, 48, v28
	v_mad_i64_i32 v[4:5], s[18:19], v3, s2, v[12:13]
	global_load_dwordx4 v[164:167], v[4:5], off
	v_add_u32_e32 v3, 52, v28
	v_mad_i64_i32 v[4:5], s[18:19], v3, s2, v[12:13]
	global_load_dwordx4 v[168:171], v[4:5], off
	v_add_u32_e32 v3, 56, v28
	v_mad_i64_i32 v[4:5], s[18:19], v3, s2, v[12:13]
	global_load_dwordx4 v[172:175], v[4:5], off
	v_add_u32_e32 v3, 60, v28
	v_mad_i64_i32 v[4:5], s[18:19], v3, s2, v[12:13]
	global_load_dwordx4 v[176:179], v[4:5], off
.Ltr_ld_done:
	s_or_b64 exec, exec, s[14:15]
	s_waitcnt vmcnt(15)
	v_mov_b32_e32 v6, v29
	ds_write2_b32 v6, v116, v117 offset1:1
	ds_write2_b32 v6, v118, v119 offset0:2 offset1:3
	s_waitcnt vmcnt(14)
	v_add_u32_e32 v6, 0x410, v29
	ds_write2_b32 v6, v120, v121 offset1:1
	ds_write2_b32 v6, v122, v123 offset0:2 offset1:3
	s_waitcnt vmcnt(13)
	v_add_u32_e32 v6, 0x820, v29
	ds_write2_b32 v6, v124, v125 offset1:1
	ds_write2_b32 v6, v126, v127 offset0:2 offset1:3
	s_waitcnt vmcnt(12)
	v_add_u32_e32 v6, 0xc30, v29
	ds_write2_b32 v6, v128, v129 offset1:1
	ds_write2_b32 v6, v130, v131 offset0:2 offset1:3
	s_waitcnt vmcnt(11)
	v_add_u32_e32 v6, 0x1040, v29
	ds_write2_b32 v6, v132, v133 offset1:1
	ds_write2_b32 v6, v134, v135 offset0:2 offset1:3
	s_waitcnt vmcnt(10)
	v_add_u32_e32 v6, 0x1450, v29
	ds_write2_b32 v6, v136, v137 offset1:1
	ds_write2_b32 v6, v138, v139 offset0:2 offset1:3
	s_waitcnt vmcnt(9)
	v_add_u32_e32 v6, 0x1860, v29
	ds_write2_b32 v6, v140, v141 offset1:1
	ds_write2_b32 v6, v142, v143 offset0:2 offset1:3
	s_waitcnt vmcnt(8)
	v_add_u32_e32 v6, 0x1c70, v29
	ds_write2_b32 v6, v144, v145 offset1:1
	ds_write2_b32 v6, v146, v147 offset0:2 offset1:3
	s_waitcnt vmcnt(7)
	v_add_u32_e32 v6, 0x2080, v29
	ds_write2_b32 v6, v148, v149 offset1:1
	ds_write2_b32 v6, v150, v151 offset0:2 offset1:3
	s_waitcnt vmcnt(6)
	v_add_u32_e32 v6, 0x2490, v29
	ds_write2_b32 v6, v152, v153 offset1:1
	ds_write2_b32 v6, v154, v155 offset0:2 offset1:3
	s_waitcnt vmcnt(5)
	v_add_u32_e32 v6, 0x28a0, v29
	ds_write2_b32 v6, v156, v157 offset1:1
	ds_write2_b32 v6, v158, v159 offset0:2 offset1:3
	s_waitcnt vmcnt(4)
	v_add_u32_e32 v6, 0x2cb0, v29
	ds_write2_b32 v6, v160, v161 offset1:1
	ds_write2_b32 v6, v162, v163 offset0:2 offset1:3
	s_waitcnt vmcnt(3)
	v_add_u32_e32 v6, 0x30c0, v29
	ds_write2_b32 v6, v164, v165 offset1:1
	ds_write2_b32 v6, v166, v167 offset0:2 offset1:3
	s_waitcnt vmcnt(2)
	v_add_u32_e32 v6, 0x34d0, v29
	ds_write2_b32 v6, v168, v169 offset1:1
	ds_write2_b32 v6, v170, v171 offset0:2 offset1:3
	s_waitcnt vmcnt(1)
	v_add_u32_e32 v6, 0x38e0, v29
	ds_write2_b32 v6, v172, v173 offset1:1
	ds_write2_b32 v6, v174, v175 offset0:2 offset1:3
	s_waitcnt vmcnt(0)
	v_add_u32_e32 v6, 0x3cf0, v29
	ds_write2_b32 v6, v176, v177 offset1:1
	ds_write2_b32 v6, v178, v179 offset0:2 offset1:3
	s_branch .LBB0_15
